# mixer queue: wait for the claim-ahead atomic deferred to the end of the entry (returns into v248)
# speedup vs baseline: 1.0030x; 1.0030x over previous
.LBB0_896:
	v_readlane_b32 s10, v254, 15
	v_readlane_b32 s11, v254, 16
	v_cmp_eq_u32_e64 s[36:37], 0, v212
	s_and_b64 s[20:21], s[10:11], s[36:37]
	s_and_saveexec_b64 s[38:39], s[20:21]
	s_cbranch_execz .LBB0_900
	s_mov_b64 s[42:43], exec
	v_mbcnt_lo_u32_b32 v0, s42, 0
	v_mbcnt_hi_u32_b32 v0, s43, v0
	v_cmp_eq_u32_e32 vcc, 0, v0
	s_and_saveexec_b64 s[40:41], vcc
	s_cbranch_execz .LBB0_899
	s_bcnt1_i32_b64 s8, s[42:43]
	v_readlane_b32 s10, v255, 38
	v_mov_b32_e32 v2, s8
	v_readlane_b32 s11, v255, 39
	s_nop 4
	global_atomic_add v248, v1, v2, s[10:11] sc0
.LBB0_899:
	s_or_b64 exec, exec, s[40:41]
.LBB0_900:
	s_or_b64 exec, exec, s[38:39]
	s_cmp_ge_u32 s7, s79
	s_mov_b64 s[38:39], -1
	s_cbranch_scc0 .LBB0_916
	s_sub_i32 s28, s7, s27
	s_mov_b32 s26, -1
	s_cbranch_execz .LBB0_917

.LBB0_1549:
	s_barrier
	s_and_saveexec_b64 s[36:37], s[20:21]
	s_cbranch_execz .LBB0_895
	s_waitcnt vmcnt(0)
	v_readlane_b32 s7, v255, 15
	s_nop 1
	v_mov_b32_e32 v0, s7
	ds_write_b32 v0, v248
	s_branch .LBB0_895
